# tile_loop: the conversion-queue fetch_add for the next job issued at the top of the iteration so its round trip overlaps the pack stage
# speedup vs baseline: 1.0010x; 1.0004x over previous
.LBB0_69:
	s_and_saveexec_b64 s[98:99], s[0:1]
	s_cbranch_execz .Lmy_tq_3
	v_mov_b32_e32 v247, 1
	global_atomic_add v247, v69, v247, s[2:3] sc0
.Lmy_tq_3:
	s_or_b64 exec, exec, s[98:99]
	s_cmp_lg_u64 s[42:43], 0
	s_cselect_b64 s[6:7], -1, 0
	s_cmp_eq_u64 s[42:43], 0
	v_mov_b32_e32 v65, 1.0
	v_mov_b32_e32 v64, 1.0
	s_cbranch_scc1 .LBB0_71
	s_add_u32 s4, s42, s38
	s_addc_u32 s5, s43, s39
	global_load_dword v64, v69, s[4:5]

.LBB0_118:
	s_mov_b64 s[8:9], exec
	v_mbcnt_lo_u32_b32 v0, s8, 0
	v_mbcnt_hi_u32_b32 v0, s9, v0
	v_cmp_eq_u32_e32 vcc, 0, v0
	s_and_saveexec_b64 s[6:7], vcc
	s_cbranch_execz .LBB0_120
	s_nop 0
	s_nop 0
	v_mov_b32_e32 v1, v247

.LBB0_1017:
	s_and_saveexec_b64 s[98:99], s[38:39]
	s_cbranch_execz .Lmy_tq_2
	v_mov_b32_e32 v247, 1
	global_atomic_add v247, v173, v247, s[0:1] sc0
.Lmy_tq_2:
	s_or_b64 exec, exec, s[98:99]
	s_cmp_lg_u64 s[20:21], 0
	s_cselect_b64 s[18:19], -1, 0
	s_cmp_eq_u64 s[20:21], 0
	v_mov_b32_e32 v65, 1.0
	v_mov_b32_e32 v64, 1.0
	s_cbranch_scc1 .LBB0_1019
	s_lshl_b64 s[22:23], s[16:17], 2
	s_add_u32 s22, s20, s22
	s_addc_u32 s23, s21, s23
	global_load_dword v64, v173, s[22:23]

.LBB0_1066:
	s_mov_b64 s[24:25], exec
	v_mbcnt_lo_u32_b32 v0, s24, 0
	v_mbcnt_hi_u32_b32 v0, s25, v0
	v_cmp_eq_u32_e32 vcc, 0, v0
	s_and_saveexec_b64 s[22:23], vcc
	s_cbranch_execz .LBB0_1068
	s_nop 0
	s_nop 0
	v_mov_b32_e32 v1, v247

.LBB0_1524:
	s_and_saveexec_b64 s[98:99], s[36:37]
	s_cbranch_execz .Lmy_tq_1
	v_mov_b32_e32 v247, 1
	global_atomic_add v247, v173, v247, s[0:1] sc0
.Lmy_tq_1:
	s_or_b64 exec, exec, s[98:99]
	s_cmp_lg_u64 s[26:27], 0
	s_cselect_b64 s[24:25], -1, 0
	s_cmp_eq_u64 s[26:27], 0
	v_mov_b32_e32 v65, 1.0
	v_mov_b32_e32 v64, 1.0
	s_cbranch_scc1 .LBB0_1526
	s_lshl_b64 s[16:17], s[22:23], 2
	s_add_u32 s16, s26, s16
	s_addc_u32 s17, s27, s17
	global_load_dword v64, v173, s[16:17]

.LBB0_1573:
	s_mov_b64 s[30:31], exec
	v_mbcnt_lo_u32_b32 v0, s30, 0
	v_mbcnt_hi_u32_b32 v0, s31, v0
	v_cmp_eq_u32_e32 vcc, 0, v0
	s_and_saveexec_b64 s[28:29], vcc
	s_cbranch_execz .LBB0_1575
	s_nop 0
	s_nop 0
	v_mov_b32_e32 v1, v247

.LBB0_1724:
	s_and_saveexec_b64 s[98:99], s[34:35]
	s_cbranch_execz .Lmy_tq_0
	v_mov_b32_e32 v247, 1
	global_atomic_add v247, v173, v247, s[0:1] sc0
.Lmy_tq_0:
	s_or_b64 exec, exec, s[98:99]
	s_cmp_lg_u64 s[30:31], 0
	s_cselect_b64 s[38:39], -1, 0
	s_cmp_eq_u64 s[30:31], 0
	v_mov_b32_e32 v65, 1.0
	v_mov_b32_e32 v64, 1.0
	s_cbranch_scc1 .LBB0_1726
	s_lshl_b64 s[14:15], s[28:29], 2
	s_add_u32 s14, s30, s14
	s_addc_u32 s15, s31, s15
	global_load_dword v64, v173, s[14:15]

.LBB0_1773:
	s_mov_b64 s[40:41], exec
	v_mbcnt_lo_u32_b32 v0, s40, 0
	v_mbcnt_hi_u32_b32 v0, s41, v0
	v_cmp_eq_u32_e32 vcc, 0, v0
	s_and_saveexec_b64 s[36:37], vcc
	s_cbranch_execz .LBB0_1775
	s_nop 0
	s_nop 0
	v_mov_b32_e32 v1, v247
